# epilogue load hoists and pipelining (P3 P6 P7 P10 P11), paired zeroing, conversion-loop drain removed; no attention-loop edits
# baseline (speedup 1.0000x reference)
; __device__ __forceinline__ cgptr cuni(const void* p) { const unsigned long long v = (unsigned long long)p; const unsigned lo = __builtin_amdgcn_readfirstlane((unsigned)v), hi = __builtin_amdgcn_readfirstlane((unsigned)(v >> 32)); return (cgptr)(((unsigned long long)hi << 32) | lo); }
; __device__ __forceinline__ ConvItem conv_decode(int it, const float* wgu, const float* wd, unsigned char* WguT, unsigned char* WdT) {
;     constexpr int I_GU = NE * 16 * 128;
;     ConvItem c; int r = it, nbn, N; const float* src; unsigned char* dstp; bool gu;
;     if (r < I_GU) { const int e = r / (16 * 128); r -= e * (16 * 128); N = 4096; nbn = 128; src = wgu + (size_t)e * DM * 4096; dstp = WguT + (size_t)e * 4096 * DM; gu = true; }
;     else { r -= I_GU; const int e = r / (16 * 64); r -= e * (16 * 64); N = DM; nbn = 64; src = wd + (size_t)e * DFF * DM; dstp = WdT + (size_t)e * DM * DFF; gu = false; }
;     const int kb = r / nbn, nb = r - kb * nbn, n0 = nb * 32, k0 = kb * 128; int dst = n0;
;     if (gu) { const int j = n0 & 2047; dst = (j >> 7) * 256 + (j & 127) + ((n0 >= 2048) ? 128 : 0); }
;     c.src = cuni(src + (size_t)k0 * N + n0); c.dstp = cuni(dstp + (size_t)dst * DM + k0); c.N4 = (unsigned)N * 4u;
;     return c;
; }
.LBB0_494:
	v_cvt_f32_ubyte0_e32 v64, s10
	v_rcp_iflag_f32_e32 v64, v64
	s_sub_i32 s17, 0, s10
	s_abs_i32 s12, s9
	s_ashr_i32 s11, s9, 31
	v_mul_f32_e32 v64, 0x4f7ffffe, v64
	v_cvt_u32_f32_e32 v64, v64
	v_add_u32_e32 v152, 0x400, v148
	v_add_u32_e32 v153, 0x400, v149
	v_add_u32_e32 v154, 0x400, v150
	v_readfirstlane_b32 s26, v64
	s_mul_i32 s17, s17, s26
	s_mul_hi_u32 s17, s26, s17
	s_add_i32 s26, s26, s17
	s_mul_hi_u32 s17, s12, s26
	s_mul_i32 s26, s17, s10
	s_sub_i32 s12, s12, s26
	s_add_i32 s27, s17, 1
	s_sub_i32 s26, s12, s10
	s_cmp_ge_u32 s12, s10
	s_cselect_b32 s17, s27, s17
	s_cselect_b32 s12, s26, s12
	s_add_i32 s26, s17, 1
	s_cmp_ge_u32 s12, s10
	s_cselect_b32 s12, s26, s17
	s_xor_b32 s12, s12, s11
	s_sub_i32 s11, s12, s11
	s_mul_i32 s10, s11, s10
	s_lshl_b32 s17, s9, 6
	s_sub_i32 s9, s9, s10
	s_lshl_b32 s10, s9, 5
	s_and_b32 s12, s17, 0xf00
	s_and_b32 s17, s10, 0x60
	s_or_b32 s12, s17, s12
	s_cmp_gt_i32 s9, 63
	s_cselect_b32 s9, 0x80, 0
	s_or_b32 s9, s12, s9
	s_and_b64 s[18:19], s[18:19], exec
	s_cselect_b32 s18, s9, s10
	s_lshl_b32 s9, s11, 7
	s_mul_hi_i32 s27, s9, s8
	s_mul_i32 s26, s9, s8
	s_ashr_i32 s12, s9, 31
	s_lshl_b64 s[26:27], s[26:27], 2
	s_add_u32 s17, s24, s26
	s_addc_u32 s19, s25, s27
	s_ashr_i32 s11, s10, 31
	s_lshl_b64 s[10:11], s[10:11], 2
	s_add_u32 s24, s17, s10
	s_addc_u32 s25, s19, s11
	s_ashr_i32 s19, s18, 31
	s_lshl_b64 s[10:11], s[18:19], 11
	s_add_u32 s10, s22, s10
	s_addc_u32 s11, s23, s11
	s_add_u32 s18, s10, s9
	s_addc_u32 s19, s11, s12
	s_lshl_b32 s9, s8, 5
	v_mul_lo_u32 v64, v130, s8
	s_add_u32 s10, s24, s9
	v_or_b32_e32 v64, v64, v131
	s_addc_u32 s11, s25, 0
	s_lshl_b32 s9, s8, 6
	global_load_dwordx4 v[124:127], v64, s[24:25] nt
	global_load_dwordx4 v[116:119], v64, s[10:11] nt
	s_add_u32 s10, s24, s9
	s_addc_u32 s11, s25, 0
	s_mul_i32 s9, s8, 0x60
	s_add_u32 s22, s24, s9
	s_addc_u32 s23, s25, 0
	s_lshl_b32 s9, s8, 7
	global_load_dwordx4 v[120:123], v64, s[10:11] nt
	global_load_dwordx4 v[108:111], v64, s[22:23] nt
	s_add_u32 s10, s24, s9
	s_addc_u32 s11, s25, 0
	s_mul_i32 s9, s8, 0xa0
	s_add_u32 s22, s24, s9
	s_addc_u32 s23, s25, 0
	s_mul_i32 s9, s8, 0xc0
	global_load_dwordx4 v[112:115], v64, s[10:11] nt
	global_load_dwordx4 v[100:103], v64, s[22:23] nt
	s_add_u32 s10, s24, s9
	s_addc_u32 s11, s25, 0
	s_mul_i32 s9, s8, 0xe0
	s_add_u32 s22, s24, s9
	s_addc_u32 s23, s25, 0
	s_lshl_b32 s9, s8, 8
	global_load_dwordx4 v[104:107], v64, s[10:11] nt
	global_load_dwordx4 v[92:95], v64, s[22:23] nt
	s_add_u32 s10, s24, s9
	s_addc_u32 s11, s25, 0
	s_mul_i32 s9, s8, 0x120
	s_add_u32 s22, s24, s9
	s_addc_u32 s23, s25, 0
	s_mul_i32 s9, s8, 0x140
	global_load_dwordx4 v[96:99], v64, s[10:11] nt
	global_load_dwordx4 v[84:87], v64, s[22:23] nt
	s_add_u32 s10, s24, s9
	s_addc_u32 s11, s25, 0
	s_mul_i32 s9, s8, 0x160
	s_add_u32 s22, s24, s9
	s_addc_u32 s23, s25, 0
	s_mul_i32 s9, s8, 0x180
	global_load_dwordx4 v[88:91], v64, s[10:11] nt
	global_load_dwordx4 v[76:79], v64, s[22:23] nt
	s_add_u32 s10, s24, s9
	s_addc_u32 s11, s25, 0
	s_mul_i32 s9, s8, 0x1a0
	s_add_u32 s22, s24, s9
	s_addc_u32 s23, s25, 0
	s_mul_i32 s9, s8, 0x1c0
	global_load_dwordx4 v[80:83], v64, s[10:11] nt
	global_load_dwordx4 v[68:71], v64, s[22:23] nt
	s_add_u32 s10, s24, s9
	s_addc_u32 s11, s25, 0
	s_mulk_i32 s8, 0x1e0
	s_add_u32 s8, s24, s8
	s_waitcnt vmcnt(29)
	v_pk_mul_f32 v[6:7], v[6:7], s[16:17] op_sel_hi:[1,0]
	v_pk_mul_f32 v[4:5], v[4:5], s[16:17] op_sel_hi:[1,0]
	s_waitcnt vmcnt(28)
	v_pk_mul_f32 v[2:3], v[2:3], s[16:17] op_sel_hi:[1,0]
	v_pk_mul_f32 v[0:1], v[0:1], s[16:17] op_sel_hi:[1,0]
	s_addc_u32 s9, s25, 0
	global_load_dwordx4 v[72:75], v64, s[10:11] nt
	s_nop 0
	global_load_dwordx4 v[64:67], v64, s[8:9] nt
	ds_write_b128 v132, v[4:7]
	ds_write_b128 v133, v[0:3]
	s_waitcnt vmcnt(29)
	v_pk_mul_f32 v[2:3], v[14:15], s[16:17] op_sel_hi:[1,0]
	v_pk_mul_f32 v[0:1], v[12:13], s[16:17] op_sel_hi:[1,0]
	ds_write_b128 v134, v[0:3]
	s_waitcnt vmcnt(28)
	v_pk_mul_f32 v[2:3], v[10:11], s[16:17] op_sel_hi:[1,0]
	v_pk_mul_f32 v[0:1], v[8:9], s[16:17] op_sel_hi:[1,0]
	ds_write_b128 v135, v[0:3]
	s_waitcnt vmcnt(27)
	v_pk_mul_f32 v[2:3], v[22:23], s[16:17] op_sel_hi:[1,0]
	v_pk_mul_f32 v[0:1], v[20:21], s[16:17] op_sel_hi:[1,0]
	ds_write_b128 v136, v[0:3]
	s_waitcnt vmcnt(26)
	v_pk_mul_f32 v[2:3], v[18:19], s[16:17] op_sel_hi:[1,0]
	v_pk_mul_f32 v[0:1], v[16:17], s[16:17] op_sel_hi:[1,0]
	ds_write_b128 v137, v[0:3]
	s_waitcnt vmcnt(25)
	v_pk_mul_f32 v[2:3], v[30:31], s[16:17] op_sel_hi:[1,0]
	v_pk_mul_f32 v[0:1], v[28:29], s[16:17] op_sel_hi:[1,0]
	ds_write_b128 v138, v[0:3]
	s_waitcnt vmcnt(24)
	v_pk_mul_f32 v[2:3], v[26:27], s[16:17] op_sel_hi:[1,0]
	v_pk_mul_f32 v[0:1], v[24:25], s[16:17] op_sel_hi:[1,0]
	ds_write_b128 v139, v[0:3]
	s_waitcnt vmcnt(23)
	v_pk_mul_f32 v[2:3], v[38:39], s[16:17] op_sel_hi:[1,0]
	v_pk_mul_f32 v[0:1], v[36:37], s[16:17] op_sel_hi:[1,0]
	ds_write_b128 v140, v[0:3]
	s_waitcnt vmcnt(22)
	v_pk_mul_f32 v[2:3], v[34:35], s[16:17] op_sel_hi:[1,0]
	v_pk_mul_f32 v[0:1], v[32:33], s[16:17] op_sel_hi:[1,0]
	ds_write_b128 v141, v[0:3]
	s_waitcnt vmcnt(21)
	v_pk_mul_f32 v[2:3], v[46:47], s[16:17] op_sel_hi:[1,0]
	v_pk_mul_f32 v[0:1], v[44:45], s[16:17] op_sel_hi:[1,0]
	ds_write_b128 v142, v[0:3]
	s_waitcnt vmcnt(20)
	v_pk_mul_f32 v[2:3], v[42:43], s[16:17] op_sel_hi:[1,0]
	v_pk_mul_f32 v[0:1], v[40:41], s[16:17] op_sel_hi:[1,0]
	ds_write_b128 v143, v[0:3]
	s_waitcnt vmcnt(19)
; #define LAS __attribute__((address_space(3)))
; #define CONV_LOAD(v, c) do { const unsigned lo_ = (unsigned)(lane >> 3) * (c).N4 + 16u * (unsigned)(lane & 7); _Pragma("unroll") for (int i = 0; i < 16; ++i) v[i] = __builtin_nontemporal_load((const GAS f32x4*)(cuni((const void*)((c).src + (size_t)(8 * i) * (c).N4)) + lo_)); } while (0)
; __device__ __forceinline__ void convert_expert_weights(const float* wgu, const float* wd, unsigned char* WguT, unsigned char* WdT, LAS float* scr, int gw, int NGW, int NIT, int lane) {
;     int it = gw; if (it >= NIT) return;
;     f32x4 va[16], vb[16];
;     ConvItem ca = conv_decode(it, wgu, wd, WguT, WdT), cb = ca;
;     CONV_LOAD(va, ca);
;     for (;;) {
;         const bool hb = it + NGW < NIT; cb = conv_decode(hb ? it + NGW : it, wgu, wd, WguT, WdT); CONV_LOAD(vb, cb);
;         CONV_STORE(va, ca);
;         if (!hb) break;
;         it += NGW;
;         const bool ha = it + NGW < NIT; ca = conv_decode(ha ? it + NGW : it, wgu, wd, WguT, WdT); CONV_LOAD(va, ca);
;         CONV_STORE(vb, cb);
;         if (!ha) break;
;         it += NGW;
;     }
	v_pk_mul_f32 v[2:3], v[54:55], s[16:17] op_sel_hi:[1,0]
	v_pk_mul_f32 v[0:1], v[52:53], s[16:17] op_sel_hi:[1,0]
	ds_write_b128 v144, v[0:3]
	s_waitcnt vmcnt(18)
	v_pk_mul_f32 v[2:3], v[50:51], s[16:17] op_sel_hi:[1,0]
	v_pk_mul_f32 v[0:1], v[48:49], s[16:17] op_sel_hi:[1,0]
	ds_write_b128 v145, v[0:3]
	s_waitcnt vmcnt(17)
	v_pk_mul_f32 v[2:3], v[62:63], s[16:17] op_sel_hi:[1,0]
	v_pk_mul_f32 v[0:1], v[60:61], s[16:17] op_sel_hi:[1,0]
	ds_write_b128 v146, v[0:3]
	s_waitcnt vmcnt(16)
	v_pk_mul_f32 v[2:3], v[58:59], s[16:17] op_sel_hi:[1,0]
	v_pk_mul_f32 v[0:1], v[56:57], s[16:17] op_sel_hi:[1,0]
	ds_write_b128 v147, v[0:3]
	s_waitcnt lgkmcnt(0)
	ds_read2_b32 v[0:1], v148 offset1:32
	ds_read2_b32 v[8:9], v148 offset0:64 offset1:96
	s_add_u32 s8, s14, 0x4000
	v_mov_b32_e32 v4, v3
	s_waitcnt lgkmcnt(0)
	v_cvt_pk_fp8_f32 v4, v0, v1
	ds_read2_b32 v[0:1], v148 offset0:128 offset1:160
	ds_read2_b32 v[10:11], v148 offset0:192 offset1:224
	v_mov_b32_e32 v5, v3
	ds_read2_b32 v[12:13], v152 offset1:32
	v_mov_b32_e32 v6, v3
	s_waitcnt lgkmcnt(2)
	v_cvt_pk_fp8_f32 v5, v0, v1
	ds_read2_b32 v[0:1], v152 offset0:64 offset1:96
	ds_read2_b32 v[14:15], v152 offset0:128 offset1:160
	v_mov_b32_e32 v7, v3
	s_waitcnt lgkmcnt(2)
	v_cvt_pk_fp8_f32 v6, v12, v13
	ds_read2_b32 v[12:13], v152 offset0:192 offset1:224
	v_cvt_pk_fp8_f32 v4, v8, v9 op_sel:[0,0,1]
	s_waitcnt lgkmcnt(1)
	v_cvt_pk_fp8_f32 v7, v14, v15
	v_cvt_pk_fp8_f32 v5, v10, v11 op_sel:[0,0,1]
	v_cvt_pk_fp8_f32 v6, v0, v1 op_sel:[0,0,1]
	ds_read2_b32 v[0:1], v149 offset1:32
	s_waitcnt lgkmcnt(1)
	v_cvt_pk_fp8_f32 v7, v12, v13 op_sel:[0,0,1]
	v_lshl_add_u64 v[8:9], s[14:15], 0, v[128:129]
	s_addc_u32 s9, s15, 0
	v_add_u32_e32 v155, 0x400, v151
	global_store_dwordx4 v[8:9], v[4:7], off nt
	ds_read2_b32 v[8:9], v149 offset0:64 offset1:96
	v_mov_b32_e32 v2, v3
	v_mov_b32_e32 v4, v3
	s_waitcnt lgkmcnt(1)
	v_cvt_pk_fp8_f32 v4, v0, v1
	ds_read2_b32 v[0:1], v149 offset0:128 offset1:160
	ds_read2_b32 v[10:11], v149 offset0:192 offset1:224
	v_mov_b32_e32 v5, v3
	ds_read2_b32 v[12:13], v153 offset1:32
	v_mov_b32_e32 v6, v3
	s_waitcnt lgkmcnt(2)
	v_cvt_pk_fp8_f32 v5, v0, v1
	ds_read2_b32 v[0:1], v153 offset0:64 offset1:96
	ds_read2_b32 v[14:15], v153 offset0:128 offset1:160
	v_mov_b32_e32 v7, v3
	s_waitcnt lgkmcnt(2)
	v_cvt_pk_fp8_f32 v6, v12, v13
	ds_read2_b32 v[12:13], v153 offset0:192 offset1:224
	v_cvt_pk_fp8_f32 v4, v8, v9 op_sel:[0,0,1]
	s_waitcnt lgkmcnt(1)
	v_cvt_pk_fp8_f32 v7, v14, v15
	v_cvt_pk_fp8_f32 v5, v10, v11 op_sel:[0,0,1]
	v_cvt_pk_fp8_f32 v6, v0, v1 op_sel:[0,0,1]
	ds_read2_b32 v[0:1], v150 offset1:32
	s_waitcnt lgkmcnt(1)
	v_cvt_pk_fp8_f32 v7, v12, v13 op_sel:[0,0,1]
	v_lshl_add_u64 v[8:9], s[8:9], 0, v[128:129]
	s_add_u32 s8, s14, 0x8000
	s_addc_u32 s9, s15, 0
	global_store_dwordx4 v[8:9], v[4:7], off nt
	ds_read2_b32 v[8:9], v150 offset0:64 offset1:96
	s_nop 0
	v_mov_b32_e32 v4, v3
	s_waitcnt lgkmcnt(1)
	v_cvt_pk_fp8_f32 v4, v0, v1
	ds_read2_b32 v[0:1], v150 offset0:128 offset1:160
	ds_read2_b32 v[10:11], v150 offset0:192 offset1:224
	v_mov_b32_e32 v5, v3
	ds_read2_b32 v[12:13], v154 offset1:32
	v_mov_b32_e32 v6, v3
	s_waitcnt lgkmcnt(2)
	v_cvt_pk_fp8_f32 v5, v0, v1
	ds_read2_b32 v[0:1], v154 offset0:64 offset1:96
	ds_read2_b32 v[14:15], v154 offset0:128 offset1:160
	v_mov_b32_e32 v7, v3
	s_waitcnt lgkmcnt(2)
	v_cvt_pk_fp8_f32 v6, v12, v13
	ds_read2_b32 v[12:13], v154 offset0:192 offset1:224
	v_cvt_pk_fp8_f32 v4, v8, v9 op_sel:[0,0,1]
	s_waitcnt lgkmcnt(1)
	v_cvt_pk_fp8_f32 v7, v14, v15
	v_cvt_pk_fp8_f32 v5, v10, v11 op_sel:[0,0,1]
	v_cvt_pk_fp8_f32 v6, v0, v1 op_sel:[0,0,1]
	ds_read2_b32 v[8:9], v151 offset1:32
	s_waitcnt lgkmcnt(1)
	v_cvt_pk_fp8_f32 v7, v12, v13 op_sel:[0,0,1]
	v_lshl_add_u64 v[0:1], s[8:9], 0, v[128:129]
	s_add_u32 s8, s14, 0xc000
	s_addc_u32 s9, s15, 0
	global_store_dwordx4 v[0:1], v[4:7], off nt
	v_mov_b32_e32 v0, v3
	ds_read2_b32 v[4:5], v151 offset0:64 offset1:96
	s_waitcnt lgkmcnt(1)
	v_cvt_pk_fp8_f32 v0, v8, v9
	ds_read2_b32 v[6:7], v151 offset0:128 offset1:160
	ds_read2_b32 v[8:9], v151 offset0:192 offset1:224
	ds_read2_b32 v[10:11], v155 offset1:32
	v_mov_b32_e32 v1, v3
	s_waitcnt lgkmcnt(3)
	v_cvt_pk_fp8_f32 v0, v4, v5 op_sel:[0,0,1]
	s_waitcnt lgkmcnt(2)
	v_cvt_pk_fp8_f32 v1, v6, v7
	ds_read2_b32 v[6:7], v155 offset0:128 offset1:160
	ds_read2_b32 v[12:13], v155 offset0:64 offset1:96
	s_waitcnt lgkmcnt(2)
	v_cvt_pk_fp8_f32 v2, v10, v11
	ds_read2_b32 v[10:11], v155 offset0:192 offset1:224
	v_cvt_pk_fp8_f32 v1, v8, v9 op_sel:[0,0,1]
	s_waitcnt lgkmcnt(2)
	v_cvt_pk_fp8_f32 v3, v6, v7
	s_waitcnt lgkmcnt(1)
	v_cvt_pk_fp8_f32 v2, v12, v13 op_sel:[0,0,1]
	v_lshl_add_u64 v[4:5], s[8:9], 0, v[128:129]
	s_andn2_b64 vcc, exec, s[20:21]
	s_waitcnt lgkmcnt(0)
	v_cvt_pk_fp8_f32 v3, v10, v11 op_sel:[0,0,1]
	s_mov_b64 s[20:21], -1
	global_store_dwordx4 v[4:5], v[0:3], off nt
	s_waitcnt lgkmcnt(0)
	s_cbranch_vccnz .LBB0_488
	s_add_i32 s1, s0, s1
	s_cmp_lt_i32 s1, s45
	s_cselect_b32 s1, s1, s3
	s_cmp_lt_i32 s1, 0x10000
	s_cselect_b64 s[14:15], -1, 0
	s_cmp_gt_i32 s1, 0xffff
	s_mov_b64 s[24:25], -1
	s_cbranch_scc0 .LBB0_497
	s_add_i32 s8, s1, 0xffff0000
	s_lshr_b32 s12, s8, 10
	s_and_b32 s9, s1, 0x3ff
	s_lshl_b64 s[10:11], s[12:13], 22
	s_lshl_b64 s[20:21], s[12:13], 24
	s_add_u32 s22, s6, s20
	s_addc_u32 s23, s7, s21
	s_add_u32 s20, s77, s10
	v_readlane_b32 s8, v252, 33
	s_addc_u32 s21, s8, s11
	s_mov_b64 s[24:25], 0

; __device__ __forceinline__ cgptr cuni(const void* p) { const unsigned long long v = (unsigned long long)p; const unsigned lo = __builtin_amdgcn_readfirstlane((unsigned)v), hi = __builtin_amdgcn_readfirstlane((unsigned)(v >> 32)); return (cgptr)(((unsigned long long)hi << 32) | lo); }
; __device__ __forceinline__ ConvItem conv_decode(int it, const float* wgu, const float* wd, unsigned char* WguT, unsigned char* WdT) {
;     constexpr int I_GU = NE * 16 * 128;
;     ConvItem c; int r = it, nbn, N; const float* src; unsigned char* dstp; bool gu;
;     if (r < I_GU) { const int e = r / (16 * 128); r -= e * (16 * 128); N = 4096; nbn = 128; src = wgu + (size_t)e * DM * 4096; dstp = WguT + (size_t)e * 4096 * DM; gu = true; }
;     else { r -= I_GU; const int e = r / (16 * 64); r -= e * (16 * 64); N = DM; nbn = 64; src = wd + (size_t)e * DFF * DM; dstp = WdT + (size_t)e * DM * DFF; gu = false; }
;     const int kb = r / nbn, nb = r - kb * nbn, n0 = nb * 32, k0 = kb * 128; int dst = n0;
;     if (gu) { const int j = n0 & 2047; dst = (j >> 7) * 256 + (j & 127) + ((n0 >= 2048) ? 128 : 0); }
;     c.src = cuni(src + (size_t)k0 * N + n0); c.dstp = cuni(dstp + (size_t)dst * DM + k0); c.N4 = (unsigned)N * 4u;
;     return c;
; }
.LBB0_564:
	v_cvt_f32_ubyte0_e32 v64, s12
	v_rcp_iflag_f32_e32 v64, v64
	s_sub_i32 s27, 0, s12
	s_abs_i32 s26, s9
	s_ashr_i32 s17, s9, 31
	v_mul_f32_e32 v64, 0x4f7ffffe, v64
	v_cvt_u32_f32_e32 v64, v64
	v_add_u32_e32 v152, 0x400, v148
	v_add_u32_e32 v153, 0x400, v149
	v_add_u32_e32 v154, 0x400, v150
	v_readfirstlane_b32 s30, v64
	s_mul_i32 s27, s27, s30
	s_mul_hi_u32 s27, s30, s27
	s_add_i32 s30, s30, s27
	s_mul_hi_u32 s27, s26, s30
	s_mul_i32 s30, s27, s12
	s_sub_i32 s26, s26, s30
	s_add_i32 s31, s27, 1
	s_sub_i32 s30, s26, s12
	s_cmp_ge_u32 s26, s12
	s_cselect_b32 s27, s31, s27
	s_cselect_b32 s26, s30, s26
	s_add_i32 s30, s27, 1
	s_cmp_ge_u32 s26, s12
	s_cselect_b32 s26, s30, s27
	s_xor_b32 s26, s26, s17
	s_sub_i32 s17, s26, s17
	s_mul_i32 s12, s17, s12
	s_lshl_b32 s27, s9, 6
	s_sub_i32 s9, s9, s12
	s_lshl_b32 s26, s9, 5
	s_and_b32 s12, s27, 0xf00
	s_and_b32 s27, s26, 0x60
	s_or_b32 s12, s27, s12
	s_cmp_gt_i32 s9, 63
	s_cselect_b32 s9, 0x80, 0
	s_or_b32 s9, s12, s9
	s_and_b64 s[18:19], s[18:19], exec
	s_cselect_b32 s18, s9, s26
	s_lshl_b32 s9, s17, 7
	s_mul_hi_i32 s31, s9, s8
	s_mul_i32 s30, s9, s8
	s_ashr_i32 s12, s9, 31
	s_lshl_b64 s[30:31], s[30:31], 2
	s_add_u32 s17, s24, s30
	s_addc_u32 s19, s25, s31
	s_ashr_i32 s27, s26, 31
	s_lshl_b64 s[24:25], s[26:27], 2
	s_add_u32 s24, s17, s24
	s_addc_u32 s25, s19, s25
	s_ashr_i32 s19, s18, 31
	s_lshl_b64 s[18:19], s[18:19], 11
	s_add_u32 s17, s22, s18
	s_addc_u32 s19, s23, s19
	s_add_u32 s18, s17, s9
	s_addc_u32 s19, s19, s12
	s_lshl_b32 s9, s8, 5
	v_mul_lo_u32 v64, v130, s8
	s_add_u32 s22, s24, s9
	v_or_b32_e32 v64, v64, v131
	s_addc_u32 s23, s25, 0
	s_lshl_b32 s9, s8, 6
	global_load_dwordx4 v[124:127], v64, s[24:25] nt
	global_load_dwordx4 v[116:119], v64, s[22:23] nt
	s_add_u32 s22, s24, s9
	s_addc_u32 s23, s25, 0
	s_mul_i32 s9, s8, 0x60
	s_add_u32 s26, s24, s9
	s_addc_u32 s27, s25, 0
	s_lshl_b32 s9, s8, 7
	global_load_dwordx4 v[120:123], v64, s[22:23] nt
	global_load_dwordx4 v[108:111], v64, s[26:27] nt
	s_add_u32 s22, s24, s9
	s_addc_u32 s23, s25, 0
	s_mul_i32 s9, s8, 0xa0
	s_add_u32 s26, s24, s9
	s_addc_u32 s27, s25, 0
	s_mul_i32 s9, s8, 0xc0
	global_load_dwordx4 v[112:115], v64, s[22:23] nt
	global_load_dwordx4 v[100:103], v64, s[26:27] nt
	s_add_u32 s22, s24, s9
	s_addc_u32 s23, s25, 0
	s_mul_i32 s9, s8, 0xe0
	s_add_u32 s26, s24, s9
	s_addc_u32 s27, s25, 0
	s_lshl_b32 s9, s8, 8
	global_load_dwordx4 v[104:107], v64, s[22:23] nt
	global_load_dwordx4 v[92:95], v64, s[26:27] nt
	s_add_u32 s22, s24, s9
	s_addc_u32 s23, s25, 0
	s_mul_i32 s9, s8, 0x120
	s_add_u32 s26, s24, s9
	s_addc_u32 s27, s25, 0
	s_mul_i32 s9, s8, 0x140
	global_load_dwordx4 v[96:99], v64, s[22:23] nt
	global_load_dwordx4 v[84:87], v64, s[26:27] nt
	s_add_u32 s22, s24, s9
	s_addc_u32 s23, s25, 0
	s_mul_i32 s9, s8, 0x160
	s_add_u32 s26, s24, s9
	s_addc_u32 s27, s25, 0
	s_mul_i32 s9, s8, 0x180
	global_load_dwordx4 v[88:91], v64, s[22:23] nt
	global_load_dwordx4 v[76:79], v64, s[26:27] nt
	s_add_u32 s22, s24, s9
	s_addc_u32 s23, s25, 0
	s_mul_i32 s9, s8, 0x1a0
	s_add_u32 s26, s24, s9
	s_addc_u32 s27, s25, 0
	s_mul_i32 s9, s8, 0x1c0
	global_load_dwordx4 v[80:83], v64, s[22:23] nt
	global_load_dwordx4 v[68:71], v64, s[26:27] nt
	s_add_u32 s22, s24, s9
	s_addc_u32 s23, s25, 0
	s_mulk_i32 s8, 0x1e0
	s_add_u32 s8, s24, s8
	s_waitcnt vmcnt(29)
	v_pk_mul_f32 v[6:7], v[6:7], s[16:17] op_sel_hi:[1,0]
	v_pk_mul_f32 v[4:5], v[4:5], s[16:17] op_sel_hi:[1,0]
	s_waitcnt vmcnt(28)
	v_pk_mul_f32 v[2:3], v[2:3], s[16:17] op_sel_hi:[1,0]
	v_pk_mul_f32 v[0:1], v[0:1], s[16:17] op_sel_hi:[1,0]
	s_addc_u32 s9, s25, 0
	global_load_dwordx4 v[72:75], v64, s[22:23] nt
	s_nop 0
	global_load_dwordx4 v[64:67], v64, s[8:9] nt
	ds_write_b128 v132, v[4:7]
	ds_write_b128 v133, v[0:3]
	s_waitcnt vmcnt(29)
	v_pk_mul_f32 v[2:3], v[14:15], s[16:17] op_sel_hi:[1,0]
	v_pk_mul_f32 v[0:1], v[12:13], s[16:17] op_sel_hi:[1,0]
	ds_write_b128 v134, v[0:3]
	s_waitcnt vmcnt(28)
	v_pk_mul_f32 v[2:3], v[10:11], s[16:17] op_sel_hi:[1,0]
	v_pk_mul_f32 v[0:1], v[8:9], s[16:17] op_sel_hi:[1,0]
	ds_write_b128 v135, v[0:3]
	s_waitcnt vmcnt(27)
	v_pk_mul_f32 v[2:3], v[22:23], s[16:17] op_sel_hi:[1,0]
	v_pk_mul_f32 v[0:1], v[20:21], s[16:17] op_sel_hi:[1,0]
	ds_write_b128 v136, v[0:3]
	s_waitcnt vmcnt(26)
	v_pk_mul_f32 v[2:3], v[18:19], s[16:17] op_sel_hi:[1,0]
	v_pk_mul_f32 v[0:1], v[16:17], s[16:17] op_sel_hi:[1,0]
	ds_write_b128 v137, v[0:3]
	s_waitcnt vmcnt(25)
	v_pk_mul_f32 v[2:3], v[30:31], s[16:17] op_sel_hi:[1,0]
	v_pk_mul_f32 v[0:1], v[28:29], s[16:17] op_sel_hi:[1,0]
	ds_write_b128 v138, v[0:3]
	s_waitcnt vmcnt(24)
	v_pk_mul_f32 v[2:3], v[26:27], s[16:17] op_sel_hi:[1,0]
	v_pk_mul_f32 v[0:1], v[24:25], s[16:17] op_sel_hi:[1,0]
	ds_write_b128 v139, v[0:3]
	s_waitcnt vmcnt(23)
	v_pk_mul_f32 v[2:3], v[38:39], s[16:17] op_sel_hi:[1,0]
	v_pk_mul_f32 v[0:1], v[36:37], s[16:17] op_sel_hi:[1,0]
	ds_write_b128 v140, v[0:3]
	s_waitcnt vmcnt(22)
	v_pk_mul_f32 v[2:3], v[34:35], s[16:17] op_sel_hi:[1,0]
	v_pk_mul_f32 v[0:1], v[32:33], s[16:17] op_sel_hi:[1,0]
	ds_write_b128 v141, v[0:3]
	s_waitcnt vmcnt(21)
	v_pk_mul_f32 v[2:3], v[46:47], s[16:17] op_sel_hi:[1,0]
	v_pk_mul_f32 v[0:1], v[44:45], s[16:17] op_sel_hi:[1,0]
	ds_write_b128 v142, v[0:3]
	s_waitcnt vmcnt(20)
	v_pk_mul_f32 v[2:3], v[42:43], s[16:17] op_sel_hi:[1,0]
	v_pk_mul_f32 v[0:1], v[40:41], s[16:17] op_sel_hi:[1,0]
	ds_write_b128 v143, v[0:3]
	s_waitcnt vmcnt(19)
; #define LAS __attribute__((address_space(3)))
; #define CONV_LOAD(v, c) do { const unsigned lo_ = (unsigned)(lane >> 3) * (c).N4 + 16u * (unsigned)(lane & 7); _Pragma("unroll") for (int i = 0; i < 16; ++i) v[i] = __builtin_nontemporal_load((const GAS f32x4*)(cuni((const void*)((c).src + (size_t)(8 * i) * (c).N4)) + lo_)); } while (0)
; __device__ __forceinline__ void convert_expert_weights(const float* wgu, const float* wd, unsigned char* WguT, unsigned char* WdT, LAS float* scr, int gw, int NGW, int NIT, int lane) {
;     int it = gw; if (it >= NIT) return;
;     f32x4 va[16], vb[16];
;     ConvItem ca = conv_decode(it, wgu, wd, WguT, WdT), cb = ca;
;     CONV_LOAD(va, ca);
;     for (;;) {
;         const bool hb = it + NGW < NIT; cb = conv_decode(hb ? it + NGW : it, wgu, wd, WguT, WdT); CONV_LOAD(vb, cb);
;         CONV_STORE(va, ca);
;         if (!hb) break;
;         it += NGW;
;         const bool ha = it + NGW < NIT; ca = conv_decode(ha ? it + NGW : it, wgu, wd, WguT, WdT); CONV_LOAD(va, ca);
;         CONV_STORE(vb, cb);
;         if (!ha) break;
;         it += NGW;
;     }
	v_pk_mul_f32 v[2:3], v[54:55], s[16:17] op_sel_hi:[1,0]
	v_pk_mul_f32 v[0:1], v[52:53], s[16:17] op_sel_hi:[1,0]
	ds_write_b128 v144, v[0:3]
	s_waitcnt vmcnt(18)
	v_pk_mul_f32 v[2:3], v[50:51], s[16:17] op_sel_hi:[1,0]
	v_pk_mul_f32 v[0:1], v[48:49], s[16:17] op_sel_hi:[1,0]
	ds_write_b128 v145, v[0:3]
	s_waitcnt vmcnt(17)
	v_pk_mul_f32 v[2:3], v[62:63], s[16:17] op_sel_hi:[1,0]
	v_pk_mul_f32 v[0:1], v[60:61], s[16:17] op_sel_hi:[1,0]
	ds_write_b128 v146, v[0:3]
	s_waitcnt vmcnt(16)
	v_pk_mul_f32 v[2:3], v[58:59], s[16:17] op_sel_hi:[1,0]
	v_pk_mul_f32 v[0:1], v[56:57], s[16:17] op_sel_hi:[1,0]
	ds_write_b128 v147, v[0:3]
	s_waitcnt lgkmcnt(0)
	ds_read2_b32 v[0:1], v148 offset1:32
	ds_read2_b32 v[8:9], v148 offset0:64 offset1:96
	s_add_u32 s8, s14, 0x4000
	v_mov_b32_e32 v4, v3
	s_waitcnt lgkmcnt(0)
	v_cvt_pk_fp8_f32 v4, v0, v1
	ds_read2_b32 v[0:1], v148 offset0:128 offset1:160
	ds_read2_b32 v[10:11], v148 offset0:192 offset1:224
	v_mov_b32_e32 v5, v3
	ds_read2_b32 v[12:13], v152 offset1:32
	v_mov_b32_e32 v6, v3
	s_waitcnt lgkmcnt(2)
	v_cvt_pk_fp8_f32 v5, v0, v1
	ds_read2_b32 v[0:1], v152 offset0:64 offset1:96
	ds_read2_b32 v[14:15], v152 offset0:128 offset1:160
	v_mov_b32_e32 v7, v3
	s_waitcnt lgkmcnt(2)
	v_cvt_pk_fp8_f32 v6, v12, v13
	ds_read2_b32 v[12:13], v152 offset0:192 offset1:224
	v_cvt_pk_fp8_f32 v4, v8, v9 op_sel:[0,0,1]
	s_waitcnt lgkmcnt(1)
	v_cvt_pk_fp8_f32 v7, v14, v15
	v_cvt_pk_fp8_f32 v5, v10, v11 op_sel:[0,0,1]
	v_cvt_pk_fp8_f32 v6, v0, v1 op_sel:[0,0,1]
	ds_read2_b32 v[0:1], v149 offset1:32
	s_waitcnt lgkmcnt(1)
	v_cvt_pk_fp8_f32 v7, v12, v13 op_sel:[0,0,1]
	v_lshl_add_u64 v[8:9], s[14:15], 0, v[128:129]
	s_addc_u32 s9, s15, 0
	v_add_u32_e32 v155, 0x400, v151
	global_store_dwordx4 v[8:9], v[4:7], off nt
	ds_read2_b32 v[8:9], v149 offset0:64 offset1:96
	v_mov_b32_e32 v2, v3
	v_mov_b32_e32 v4, v3
	s_waitcnt lgkmcnt(1)
	v_cvt_pk_fp8_f32 v4, v0, v1
	ds_read2_b32 v[0:1], v149 offset0:128 offset1:160
	ds_read2_b32 v[10:11], v149 offset0:192 offset1:224
	v_mov_b32_e32 v5, v3
	ds_read2_b32 v[12:13], v153 offset1:32
	v_mov_b32_e32 v6, v3
	s_waitcnt lgkmcnt(2)
	v_cvt_pk_fp8_f32 v5, v0, v1
	ds_read2_b32 v[0:1], v153 offset0:64 offset1:96
	ds_read2_b32 v[14:15], v153 offset0:128 offset1:160
	v_mov_b32_e32 v7, v3
	s_waitcnt lgkmcnt(2)
	v_cvt_pk_fp8_f32 v6, v12, v13
	ds_read2_b32 v[12:13], v153 offset0:192 offset1:224
	v_cvt_pk_fp8_f32 v4, v8, v9 op_sel:[0,0,1]
	s_waitcnt lgkmcnt(1)
	v_cvt_pk_fp8_f32 v7, v14, v15
	v_cvt_pk_fp8_f32 v5, v10, v11 op_sel:[0,0,1]
	v_cvt_pk_fp8_f32 v6, v0, v1 op_sel:[0,0,1]
	ds_read2_b32 v[0:1], v150 offset1:32
	s_waitcnt lgkmcnt(1)
	v_cvt_pk_fp8_f32 v7, v12, v13 op_sel:[0,0,1]
	v_lshl_add_u64 v[8:9], s[8:9], 0, v[128:129]
	s_add_u32 s8, s14, 0x8000
	s_addc_u32 s9, s15, 0
	global_store_dwordx4 v[8:9], v[4:7], off nt
	ds_read2_b32 v[8:9], v150 offset0:64 offset1:96
	s_nop 0
	v_mov_b32_e32 v4, v3
	s_waitcnt lgkmcnt(1)
	v_cvt_pk_fp8_f32 v4, v0, v1
	ds_read2_b32 v[0:1], v150 offset0:128 offset1:160
	ds_read2_b32 v[10:11], v150 offset0:192 offset1:224
	v_mov_b32_e32 v5, v3
	ds_read2_b32 v[12:13], v154 offset1:32
	v_mov_b32_e32 v6, v3
	s_waitcnt lgkmcnt(2)
	v_cvt_pk_fp8_f32 v5, v0, v1
	ds_read2_b32 v[0:1], v154 offset0:64 offset1:96
	ds_read2_b32 v[14:15], v154 offset0:128 offset1:160
	v_mov_b32_e32 v7, v3
	s_waitcnt lgkmcnt(2)
	v_cvt_pk_fp8_f32 v6, v12, v13
	ds_read2_b32 v[12:13], v154 offset0:192 offset1:224
	v_cvt_pk_fp8_f32 v4, v8, v9 op_sel:[0,0,1]
	s_waitcnt lgkmcnt(1)
	v_cvt_pk_fp8_f32 v7, v14, v15
	v_cvt_pk_fp8_f32 v5, v10, v11 op_sel:[0,0,1]
	v_cvt_pk_fp8_f32 v6, v0, v1 op_sel:[0,0,1]
	ds_read2_b32 v[8:9], v151 offset1:32
	s_waitcnt lgkmcnt(1)
	v_cvt_pk_fp8_f32 v7, v12, v13 op_sel:[0,0,1]
	v_lshl_add_u64 v[0:1], s[8:9], 0, v[128:129]
	s_add_u32 s8, s14, 0xc000
	s_addc_u32 s9, s15, 0
	global_store_dwordx4 v[0:1], v[4:7], off nt
	v_mov_b32_e32 v0, v3
	ds_read2_b32 v[4:5], v151 offset0:64 offset1:96
	s_waitcnt lgkmcnt(1)
	v_cvt_pk_fp8_f32 v0, v8, v9
	ds_read2_b32 v[6:7], v151 offset0:128 offset1:160
	ds_read2_b32 v[8:9], v151 offset0:192 offset1:224
	ds_read2_b32 v[10:11], v155 offset1:32
	v_mov_b32_e32 v1, v3
	s_waitcnt lgkmcnt(3)
	v_cvt_pk_fp8_f32 v0, v4, v5 op_sel:[0,0,1]
	s_waitcnt lgkmcnt(2)
	v_cvt_pk_fp8_f32 v1, v6, v7
	ds_read2_b32 v[6:7], v155 offset0:128 offset1:160
	ds_read2_b32 v[12:13], v155 offset0:64 offset1:96
	s_waitcnt lgkmcnt(2)
	v_cvt_pk_fp8_f32 v2, v10, v11
	ds_read2_b32 v[10:11], v155 offset0:192 offset1:224
	v_cvt_pk_fp8_f32 v1, v8, v9 op_sel:[0,0,1]
	s_waitcnt lgkmcnt(2)
	v_cvt_pk_fp8_f32 v3, v6, v7
	s_waitcnt lgkmcnt(1)
	v_cvt_pk_fp8_f32 v2, v12, v13 op_sel:[0,0,1]
	v_lshl_add_u64 v[4:5], s[8:9], 0, v[128:129]
	s_andn2_b64 vcc, exec, s[20:21]
	s_waitcnt lgkmcnt(0)
	v_cvt_pk_fp8_f32 v3, v10, v11 op_sel:[0,0,1]
	s_mov_b64 s[20:21], -1
	global_store_dwordx4 v[4:5], v[0:3], off nt
	s_waitcnt lgkmcnt(0)
	s_cbranch_vccnz .LBB0_558
	s_add_i32 s1, s0, s1
	s_cmp_lt_i32 s1, s45
	s_cselect_b32 s1, s1, s3
	s_cmp_lt_i32 s1, 0x10000
	s_cselect_b64 s[14:15], -1, 0
	s_cmp_gt_i32 s1, 0xffff
	s_mov_b64 s[24:25], -1
	s_cbranch_scc0 .LBB0_567
	s_add_i32 s8, s1, 0xffff0000
	s_lshr_b32 s12, s8, 10
	s_and_b32 s9, s1, 0x3ff
	s_lshl_b64 s[20:21], s[12:13], 22
	s_lshl_b64 s[22:23], s[12:13], 24
	s_add_u32 s22, s6, s22
	s_addc_u32 s23, s7, s23
	s_add_u32 s20, s77, s20
	v_readlane_b32 s8, v252, 33
	s_addc_u32 s21, s8, s21
	s_mov_b64 s[24:25], 0

; __device__ __forceinline__ cgptr cuni(const void* p) { const unsigned long long v = (unsigned long long)p; const unsigned lo = __builtin_amdgcn_readfirstlane((unsigned)v), hi = __builtin_amdgcn_readfirstlane((unsigned)(v >> 32)); return (cgptr)(((unsigned long long)hi << 32) | lo); }
; __device__ __forceinline__ ConvItem conv_decode(int it, const float* wgu, const float* wd, unsigned char* WguT, unsigned char* WdT) {
;     constexpr int I_GU = NE * 16 * 128;
;     ConvItem c; int r = it, nbn, N; const float* src; unsigned char* dstp; bool gu;
;     if (r < I_GU) { const int e = r / (16 * 128); r -= e * (16 * 128); N = 4096; nbn = 128; src = wgu + (size_t)e * DM * 4096; dstp = WguT + (size_t)e * 4096 * DM; gu = true; }
;     else { r -= I_GU; const int e = r / (16 * 64); r -= e * (16 * 64); N = DM; nbn = 64; src = wd + (size_t)e * DFF * DM; dstp = WdT + (size_t)e * DM * DFF; gu = false; }
;     const int kb = r / nbn, nb = r - kb * nbn, n0 = nb * 32, k0 = kb * 128; int dst = n0;
;     if (gu) { const int j = n0 & 2047; dst = (j >> 7) * 256 + (j & 127) + ((n0 >= 2048) ? 128 : 0); }
;     c.src = cuni(src + (size_t)k0 * N + n0); c.dstp = cuni(dstp + (size_t)dst * DM + k0); c.N4 = (unsigned)N * 4u;
;     return c;
; }
.LBB0_764:
	v_cvt_f32_ubyte0_e32 v64, s9
	v_rcp_iflag_f32_e32 v64, v64
	s_sub_i32 s12, 0, s9
	s_abs_i32 s11, s8
	s_ashr_i32 s10, s8, 31
	v_mul_f32_e32 v64, 0x4f7ffffe, v64
	v_cvt_u32_f32_e32 v64, v64
	v_add_u32_e32 v152, 0x400, v148
	v_add_u32_e32 v153, 0x400, v149
	v_add_u32_e32 v154, 0x400, v150
	v_readfirstlane_b32 s17, v64
	s_mul_i32 s12, s12, s17
	s_mul_hi_u32 s12, s17, s12
	s_add_i32 s17, s17, s12
	s_mul_hi_u32 s12, s11, s17
	s_mul_i32 s17, s12, s9
	s_sub_i32 s11, s11, s17
	s_add_i32 s26, s12, 1
	s_sub_i32 s17, s11, s9
	s_cmp_ge_u32 s11, s9
	s_cselect_b32 s12, s26, s12
	s_cselect_b32 s11, s17, s11
	s_add_i32 s17, s12, 1
	s_cmp_ge_u32 s11, s9
	s_cselect_b32 s11, s17, s12
	s_xor_b32 s11, s11, s10
	s_sub_i32 s17, s11, s10
	s_mul_i32 s9, s17, s9
	s_sub_i32 s9, s8, s9
	s_lshl_b32 s12, s8, 6
	s_lshl_b32 s8, s9, 5
	s_and_b32 s10, s12, 0xf00
	s_and_b32 s11, s8, 0x60
	s_or_b32 s10, s11, s10
	s_cmp_gt_i32 s9, 63
	s_cselect_b32 s9, 0x80, 0
	s_or_b32 s9, s10, s9
	s_and_b64 s[10:11], s[18:19], exec
	s_cselect_b32 s10, s9, s8
	s_lshl_b32 s12, s17, 7
	s_mul_hi_i32 s19, s12, s3
	s_mul_i32 s18, s12, s3
	s_ashr_i32 s17, s12, 31
	s_lshl_b64 s[18:19], s[18:19], 2
	s_add_u32 s11, s24, s18
	s_addc_u32 s18, s25, s19
	s_ashr_i32 s9, s8, 31
	s_lshl_b64 s[8:9], s[8:9], 2
	s_add_u32 s24, s11, s8
	s_addc_u32 s25, s18, s9
	s_ashr_i32 s11, s10, 31
	s_lshl_b64 s[8:9], s[10:11], 11
	s_add_u32 s8, s22, s8
	s_addc_u32 s9, s23, s9
	s_add_u32 s18, s8, s12
	s_addc_u32 s19, s9, s17
	v_mul_lo_u32 v64, v130, s3
	s_lshl_b32 s8, s3, 5
	v_or_b32_e32 v64, v64, v131
	s_add_u32 s8, s24, s8
	s_addc_u32 s9, s25, 0
	global_load_dwordx4 v[124:127], v64, s[24:25] nt
	global_load_dwordx4 v[116:119], v64, s[8:9] nt
	s_lshl_b32 s8, s3, 6
	s_add_u32 s8, s24, s8
	s_addc_u32 s9, s25, 0
	s_mul_i32 s10, s3, 0x60
	s_add_u32 s10, s24, s10
	s_addc_u32 s11, s25, 0
	global_load_dwordx4 v[120:123], v64, s[8:9] nt
	global_load_dwordx4 v[108:111], v64, s[10:11] nt
	s_lshl_b32 s8, s3, 7
	s_add_u32 s8, s24, s8
	s_addc_u32 s9, s25, 0
	s_mul_i32 s10, s3, 0xa0
	s_add_u32 s10, s24, s10
	s_addc_u32 s11, s25, 0
	global_load_dwordx4 v[112:115], v64, s[8:9] nt
	global_load_dwordx4 v[100:103], v64, s[10:11] nt
	s_mul_i32 s8, s3, 0xc0
	s_add_u32 s8, s24, s8
	s_addc_u32 s9, s25, 0
	s_mul_i32 s10, s3, 0xe0
	s_add_u32 s10, s24, s10
	s_addc_u32 s11, s25, 0
	global_load_dwordx4 v[104:107], v64, s[8:9] nt
	global_load_dwordx4 v[92:95], v64, s[10:11] nt
	s_lshl_b32 s8, s3, 8
	s_add_u32 s8, s24, s8
	s_addc_u32 s9, s25, 0
	s_mul_i32 s10, s3, 0x120
	s_add_u32 s10, s24, s10
	s_addc_u32 s11, s25, 0
	global_load_dwordx4 v[96:99], v64, s[8:9] nt
	global_load_dwordx4 v[84:87], v64, s[10:11] nt
	s_mul_i32 s8, s3, 0x140
	s_add_u32 s8, s24, s8
	s_addc_u32 s9, s25, 0
	s_mul_i32 s10, s3, 0x160
	s_add_u32 s10, s24, s10
	s_addc_u32 s11, s25, 0
	global_load_dwordx4 v[88:91], v64, s[8:9] nt
	global_load_dwordx4 v[76:79], v64, s[10:11] nt
	s_mul_i32 s8, s3, 0x180
	s_add_u32 s8, s24, s8
	s_addc_u32 s9, s25, 0
	s_mul_i32 s10, s3, 0x1a0
	s_add_u32 s10, s24, s10
	s_addc_u32 s11, s25, 0
	global_load_dwordx4 v[80:83], v64, s[8:9] nt
	global_load_dwordx4 v[68:71], v64, s[10:11] nt
	s_mul_i32 s8, s3, 0x1c0
	s_add_u32 s8, s24, s8
	s_addc_u32 s9, s25, 0
	s_mulk_i32 s3, 0x1e0
	s_add_u32 s10, s24, s3
	s_waitcnt vmcnt(29)
	v_pk_mul_f32 v[6:7], v[6:7], s[16:17] op_sel_hi:[1,0]
	v_pk_mul_f32 v[4:5], v[4:5], s[16:17] op_sel_hi:[1,0]
	s_waitcnt vmcnt(28)
	v_pk_mul_f32 v[2:3], v[2:3], s[16:17] op_sel_hi:[1,0]
	v_pk_mul_f32 v[0:1], v[0:1], s[16:17] op_sel_hi:[1,0]
	s_addc_u32 s11, s25, 0
	global_load_dwordx4 v[72:75], v64, s[8:9] nt
	s_nop 0
	global_load_dwordx4 v[64:67], v64, s[10:11] nt
	ds_write_b128 v132, v[4:7]
	ds_write_b128 v133, v[0:3]
	s_waitcnt vmcnt(29)
	v_pk_mul_f32 v[2:3], v[14:15], s[16:17] op_sel_hi:[1,0]
	v_pk_mul_f32 v[0:1], v[12:13], s[16:17] op_sel_hi:[1,0]
	ds_write_b128 v134, v[0:3]
	s_waitcnt vmcnt(28)
	v_pk_mul_f32 v[2:3], v[10:11], s[16:17] op_sel_hi:[1,0]
	v_pk_mul_f32 v[0:1], v[8:9], s[16:17] op_sel_hi:[1,0]
	ds_write_b128 v135, v[0:3]
	s_waitcnt vmcnt(27)
	v_pk_mul_f32 v[2:3], v[22:23], s[16:17] op_sel_hi:[1,0]
	v_pk_mul_f32 v[0:1], v[20:21], s[16:17] op_sel_hi:[1,0]
	ds_write_b128 v136, v[0:3]
	s_waitcnt vmcnt(26)
	v_pk_mul_f32 v[2:3], v[18:19], s[16:17] op_sel_hi:[1,0]
	v_pk_mul_f32 v[0:1], v[16:17], s[16:17] op_sel_hi:[1,0]
	ds_write_b128 v137, v[0:3]
	s_waitcnt vmcnt(25)
	v_pk_mul_f32 v[2:3], v[30:31], s[16:17] op_sel_hi:[1,0]
	v_pk_mul_f32 v[0:1], v[28:29], s[16:17] op_sel_hi:[1,0]
	ds_write_b128 v138, v[0:3]
	s_waitcnt vmcnt(24)
	v_pk_mul_f32 v[2:3], v[26:27], s[16:17] op_sel_hi:[1,0]
	v_pk_mul_f32 v[0:1], v[24:25], s[16:17] op_sel_hi:[1,0]
	ds_write_b128 v139, v[0:3]
	s_waitcnt vmcnt(23)
	v_pk_mul_f32 v[2:3], v[38:39], s[16:17] op_sel_hi:[1,0]
	v_pk_mul_f32 v[0:1], v[36:37], s[16:17] op_sel_hi:[1,0]
	ds_write_b128 v140, v[0:3]
	s_waitcnt vmcnt(22)
	v_pk_mul_f32 v[2:3], v[34:35], s[16:17] op_sel_hi:[1,0]
	v_pk_mul_f32 v[0:1], v[32:33], s[16:17] op_sel_hi:[1,0]
	ds_write_b128 v141, v[0:3]
	s_waitcnt vmcnt(21)
	v_pk_mul_f32 v[2:3], v[46:47], s[16:17] op_sel_hi:[1,0]
	v_pk_mul_f32 v[0:1], v[44:45], s[16:17] op_sel_hi:[1,0]
	ds_write_b128 v142, v[0:3]
	s_waitcnt vmcnt(20)
	v_pk_mul_f32 v[2:3], v[42:43], s[16:17] op_sel_hi:[1,0]
	v_pk_mul_f32 v[0:1], v[40:41], s[16:17] op_sel_hi:[1,0]
	ds_write_b128 v143, v[0:3]
	s_waitcnt vmcnt(19)
; #define LAS __attribute__((address_space(3)))
; #define CONV_LOAD(v, c) do { const unsigned lo_ = (unsigned)(lane >> 3) * (c).N4 + 16u * (unsigned)(lane & 7); _Pragma("unroll") for (int i = 0; i < 16; ++i) v[i] = __builtin_nontemporal_load((const GAS f32x4*)(cuni((const void*)((c).src + (size_t)(8 * i) * (c).N4)) + lo_)); } while (0)
; __device__ __forceinline__ void convert_expert_weights(const float* wgu, const float* wd, unsigned char* WguT, unsigned char* WdT, LAS float* scr, int gw, int NGW, int NIT, int lane) {
;     int it = gw; if (it >= NIT) return;
;     f32x4 va[16], vb[16];
;     ConvItem ca = conv_decode(it, wgu, wd, WguT, WdT), cb = ca;
;     CONV_LOAD(va, ca);
;     for (;;) {
;         const bool hb = it + NGW < NIT; cb = conv_decode(hb ? it + NGW : it, wgu, wd, WguT, WdT); CONV_LOAD(vb, cb);
;         CONV_STORE(va, ca);
;         if (!hb) break;
;         it += NGW;
;         const bool ha = it + NGW < NIT; ca = conv_decode(ha ? it + NGW : it, wgu, wd, WguT, WdT); CONV_LOAD(va, ca);
;         CONV_STORE(vb, cb);
;         if (!ha) break;
;         it += NGW;
;     }
	v_pk_mul_f32 v[2:3], v[54:55], s[16:17] op_sel_hi:[1,0]
	v_pk_mul_f32 v[0:1], v[52:53], s[16:17] op_sel_hi:[1,0]
	ds_write_b128 v144, v[0:3]
	s_waitcnt vmcnt(18)
	v_pk_mul_f32 v[2:3], v[50:51], s[16:17] op_sel_hi:[1,0]
	v_pk_mul_f32 v[0:1], v[48:49], s[16:17] op_sel_hi:[1,0]
	ds_write_b128 v145, v[0:3]
	s_waitcnt vmcnt(17)
	v_pk_mul_f32 v[2:3], v[62:63], s[16:17] op_sel_hi:[1,0]
	v_pk_mul_f32 v[0:1], v[60:61], s[16:17] op_sel_hi:[1,0]
	ds_write_b128 v146, v[0:3]
	s_waitcnt vmcnt(16)
	v_pk_mul_f32 v[2:3], v[58:59], s[16:17] op_sel_hi:[1,0]
	v_pk_mul_f32 v[0:1], v[56:57], s[16:17] op_sel_hi:[1,0]
	ds_write_b128 v147, v[0:3]
	s_waitcnt lgkmcnt(0)
	ds_read2_b32 v[0:1], v148 offset1:32
	ds_read2_b32 v[8:9], v148 offset0:64 offset1:96
	s_add_u32 s8, s14, 0x4000
	v_mov_b32_e32 v4, v3
	s_waitcnt lgkmcnt(0)
	v_cvt_pk_fp8_f32 v4, v0, v1
	ds_read2_b32 v[0:1], v148 offset0:128 offset1:160
	ds_read2_b32 v[10:11], v148 offset0:192 offset1:224
	v_mov_b32_e32 v5, v3
	ds_read2_b32 v[12:13], v152 offset1:32
	v_mov_b32_e32 v6, v3
	s_waitcnt lgkmcnt(2)
	v_cvt_pk_fp8_f32 v5, v0, v1
	ds_read2_b32 v[0:1], v152 offset0:64 offset1:96
	ds_read2_b32 v[14:15], v152 offset0:128 offset1:160
	v_mov_b32_e32 v7, v3
	s_waitcnt lgkmcnt(2)
	v_cvt_pk_fp8_f32 v6, v12, v13
	ds_read2_b32 v[12:13], v152 offset0:192 offset1:224
	v_cvt_pk_fp8_f32 v4, v8, v9 op_sel:[0,0,1]
	s_waitcnt lgkmcnt(1)
	v_cvt_pk_fp8_f32 v7, v14, v15
	v_cvt_pk_fp8_f32 v5, v10, v11 op_sel:[0,0,1]
	v_cvt_pk_fp8_f32 v6, v0, v1 op_sel:[0,0,1]
	ds_read2_b32 v[0:1], v149 offset1:32
	s_waitcnt lgkmcnt(1)
	v_cvt_pk_fp8_f32 v7, v12, v13 op_sel:[0,0,1]
	v_lshl_add_u64 v[8:9], s[14:15], 0, v[128:129]
	s_addc_u32 s9, s15, 0
	v_add_u32_e32 v155, 0x400, v151
	global_store_dwordx4 v[8:9], v[4:7], off nt
	ds_read2_b32 v[8:9], v149 offset0:64 offset1:96
	v_mov_b32_e32 v2, v3
	v_mov_b32_e32 v4, v3
	s_waitcnt lgkmcnt(1)
	v_cvt_pk_fp8_f32 v4, v0, v1
	ds_read2_b32 v[0:1], v149 offset0:128 offset1:160
	ds_read2_b32 v[10:11], v149 offset0:192 offset1:224
	v_mov_b32_e32 v5, v3
	ds_read2_b32 v[12:13], v153 offset1:32
	v_mov_b32_e32 v6, v3
	s_waitcnt lgkmcnt(2)
	v_cvt_pk_fp8_f32 v5, v0, v1
	ds_read2_b32 v[0:1], v153 offset0:64 offset1:96
	ds_read2_b32 v[14:15], v153 offset0:128 offset1:160
	v_mov_b32_e32 v7, v3
	s_waitcnt lgkmcnt(2)
	v_cvt_pk_fp8_f32 v6, v12, v13
	ds_read2_b32 v[12:13], v153 offset0:192 offset1:224
	v_cvt_pk_fp8_f32 v4, v8, v9 op_sel:[0,0,1]
	s_waitcnt lgkmcnt(1)
	v_cvt_pk_fp8_f32 v7, v14, v15
	v_cvt_pk_fp8_f32 v5, v10, v11 op_sel:[0,0,1]
	v_cvt_pk_fp8_f32 v6, v0, v1 op_sel:[0,0,1]
	ds_read2_b32 v[0:1], v150 offset1:32
	s_waitcnt lgkmcnt(1)
	v_cvt_pk_fp8_f32 v7, v12, v13 op_sel:[0,0,1]
	v_lshl_add_u64 v[8:9], s[8:9], 0, v[128:129]
	s_add_u32 s8, s14, 0x8000
	s_addc_u32 s9, s15, 0
	global_store_dwordx4 v[8:9], v[4:7], off nt
	ds_read2_b32 v[8:9], v150 offset0:64 offset1:96
	s_nop 0
	v_mov_b32_e32 v4, v3
	s_waitcnt lgkmcnt(1)
	v_cvt_pk_fp8_f32 v4, v0, v1
	ds_read2_b32 v[0:1], v150 offset0:128 offset1:160
	ds_read2_b32 v[10:11], v150 offset0:192 offset1:224
	v_mov_b32_e32 v5, v3
	ds_read2_b32 v[12:13], v154 offset1:32
	v_mov_b32_e32 v6, v3
	s_waitcnt lgkmcnt(2)
	v_cvt_pk_fp8_f32 v5, v0, v1
	ds_read2_b32 v[0:1], v154 offset0:64 offset1:96
	ds_read2_b32 v[14:15], v154 offset0:128 offset1:160
	v_mov_b32_e32 v7, v3
	s_waitcnt lgkmcnt(2)
	v_cvt_pk_fp8_f32 v6, v12, v13
	ds_read2_b32 v[12:13], v154 offset0:192 offset1:224
	v_cvt_pk_fp8_f32 v4, v8, v9 op_sel:[0,0,1]
	s_waitcnt lgkmcnt(1)
	v_cvt_pk_fp8_f32 v7, v14, v15
	v_cvt_pk_fp8_f32 v5, v10, v11 op_sel:[0,0,1]
	v_cvt_pk_fp8_f32 v6, v0, v1 op_sel:[0,0,1]
	ds_read2_b32 v[8:9], v151 offset1:32
	s_waitcnt lgkmcnt(1)
	v_cvt_pk_fp8_f32 v7, v12, v13 op_sel:[0,0,1]
	v_lshl_add_u64 v[0:1], s[8:9], 0, v[128:129]
	s_add_u32 s8, s14, 0xc000
	s_addc_u32 s9, s15, 0
	global_store_dwordx4 v[0:1], v[4:7], off nt
	v_mov_b32_e32 v0, v3
	ds_read2_b32 v[4:5], v151 offset0:64 offset1:96
	s_waitcnt lgkmcnt(1)
	v_cvt_pk_fp8_f32 v0, v8, v9
	ds_read2_b32 v[6:7], v151 offset0:128 offset1:160
	ds_read2_b32 v[8:9], v151 offset0:192 offset1:224
	ds_read2_b32 v[10:11], v155 offset1:32
	v_mov_b32_e32 v1, v3
	s_waitcnt lgkmcnt(3)
	v_cvt_pk_fp8_f32 v0, v4, v5 op_sel:[0,0,1]
	s_waitcnt lgkmcnt(2)
	v_cvt_pk_fp8_f32 v1, v6, v7
	ds_read2_b32 v[6:7], v155 offset0:128 offset1:160
	ds_read2_b32 v[12:13], v155 offset0:64 offset1:96
	s_waitcnt lgkmcnt(2)
	v_cvt_pk_fp8_f32 v2, v10, v11
	ds_read2_b32 v[10:11], v155 offset0:192 offset1:224
	v_cvt_pk_fp8_f32 v1, v8, v9 op_sel:[0,0,1]
	s_waitcnt lgkmcnt(2)
	v_cvt_pk_fp8_f32 v3, v6, v7
	s_waitcnt lgkmcnt(1)
	v_cvt_pk_fp8_f32 v2, v12, v13 op_sel:[0,0,1]
	v_lshl_add_u64 v[4:5], s[8:9], 0, v[128:129]
	s_andn2_b64 vcc, exec, s[20:21]
	s_waitcnt lgkmcnt(0)
	v_cvt_pk_fp8_f32 v3, v10, v11 op_sel:[0,0,1]
	s_mov_b64 s[20:21], -1
	global_store_dwordx4 v[4:5], v[0:3], off nt
	s_waitcnt lgkmcnt(0)
	s_cbranch_vccnz .LBB0_758
	s_add_i32 s3, s0, s38
	s_cmp_lt_i32 s3, s45
	s_cselect_b32 s3, s3, s1
	s_cmp_lt_i32 s3, 0x10000
	s_cselect_b64 s[14:15], -1, 0
	s_cmp_gt_i32 s3, 0xffff
	s_mov_b64 s[24:25], -1
	s_cbranch_scc0 .LBB0_767
	s_add_i32 s8, s3, 0xffff0000
	s_lshr_b32 s12, s8, 10
	s_and_b32 s8, s3, 0x3ff
	s_lshl_b64 s[10:11], s[12:13], 22
	s_lshl_b64 s[20:21], s[12:13], 24
	s_add_u32 s22, s6, s20
	s_addc_u32 s23, s7, s21
	s_add_u32 s20, s77, s10
	v_readlane_b32 s9, v252, 33
	s_addc_u32 s21, s9, s11
	s_mov_b64 s[24:25], 0
